# P12 combine hand-written for the 256-WG grid: same items/order, lane owns 4 x 4 columns at 256-column pitch so every load/store instruction is contiguous (was 16B pieces at 64B stride)
# speedup vs baseline: 1.0183x; 1.0126x over previous
; __global__ void __launch_bounds__(512, 2) fwd_kernel(Params p) {
;     ...
;         constexpr int NI = T * (DM / 16), UN = 4;
;         for (int it0 = GT(); it0 < NI; it0 += UN * NGT) {
;             int mm[UN], cc[UN], ee[UN][4], rk[UN][4]; u32x4 xa[UN], xb[UN], y[UN][4];
; #pragma unroll
;             for (int u = 0; u < UN; ++u) { const int it = it0 + u * NGT < NI ? it0 + u * NGT : it0; mm[u] = it >> 7; cc[u] = (it & 127) * 16;
;                 const i32x4 e4 = *(const i32x4*)(tok_e + mm[u] * 4), r4 = *(const i32x4*)(tok_rank + mm[u] * 4);
; #pragma unroll
;                 for (int k = 0; k < 4; ++k) { ee[u][k] = e4[k]; rk[u][k] = r4[k]; }
;                 const bf16_t* xp = X1 + (size_t)mm[u] * DM + cc[u]; xa[u] = *(const u32x4*)xp; xb[u] = *(const u32x4*)(xp + 8); }
; #pragma unroll
;             for (int u = 0; u < UN; ++u)
; #pragma unroll
;                 for (int k = 0; k < 4; ++k) { const int pos = ts[ee[u][k]] * 256 + rk[u][k]; y[u][k] = *(const u32x4*)(Yb + (size_t)pos * DM + cc[u]); }
.LBB0_1194:
	s_or_b64 exec, exec, s[2:3]
	s_waitcnt lgkmcnt(0)
	s_barrier
	v_mbcnt_lo_u32_b32 v0, -1, 0
	v_mbcnt_hi_u32_b32 v0, -1, v0
	v_readlane_b32 s0, v252, 3
	s_nop 1
	v_add_u32_e32 v0, s0, v0
	v_readlane_b32 s0, v252, 7
	s_mov_b32 s11, 0x200000
	s_waitcnt vmcnt(9) lgkmcnt(0)
	v_add_u32_e32 v88, s0, v0
	v_cmp_gt_i32_e32 vcc, s11, v88
	s_barrier
	s_and_saveexec_b64 s[0:1], vcc
	s_cbranch_execz .LBB0_1207
	s_cmpk_lg_i32 s33, 0x100
	s_cbranch_scc1 .Lp12n_orig
	s_load_dwordx2 s[4:5], s[88:89], 0xb0
	s_mov_b32 s10, 0x3d800000
	s_mov_b32 s11, 0x3d800000
	s_add_i32 s23, 0, 0x25100
	v_and_b32_e32 v1, 63, v0
	v_bfe_u32 v2, v88, 6, 1
	v_lshrrev_b32_e32 v3, 7, v88
	v_lshlrev_b32_e32 v4, 2, v1
	v_lshl_or_b32 v4, v2, 10, v4
	v_lshlrev_b32_e32 v5, 3, v1
	v_lshl_or_b32 v5, v2, 11, v5
	v_lshlrev_b32_e32 v6, 4, v1
	v_lshl_or_b32 v6, v2, 12, v6
	s_mov_b32 s0, 0
	s_waitcnt lgkmcnt(0)
.Lp12n_loop:
	v_mov_b32_e32 v152, v3
	v_lshlrev_b32_e32 v192, 4, v152
	v_add_u32_e32 v153, 0x400, v3
	v_lshlrev_b32_e32 v193, 4, v153
	v_add_u32_e32 v154, 0x800, v3
	v_lshlrev_b32_e32 v194, 4, v154
	v_add_u32_e32 v155, 0xc00, v3
	v_lshlrev_b32_e32 v195, 4, v155
	global_load_dwordx4 v[8:11], v192, s[16:17]
	global_load_dwordx4 v[12:15], v193, s[16:17]
	global_load_dwordx4 v[16:19], v194, s[16:17]
	global_load_dwordx4 v[20:23], v195, s[16:17]
	global_load_dwordx4 v[24:27], v192, s[18:19]
	global_load_dwordx4 v[28:31], v193, s[18:19]
	global_load_dwordx4 v[32:35], v194, s[18:19]
	global_load_dwordx4 v[36:39], v195, s[18:19]
	v_lshl_add_u32 v196, v152, 12, v5
	global_load_dwordx2 v[40:41], v196, s[14:15]
	global_load_dwordx2 v[42:43], v196, s[14:15] offset:512
	global_load_dwordx2 v[44:45], v196, s[14:15] offset:1024
	global_load_dwordx2 v[46:47], v196, s[14:15] offset:1536
	v_lshl_add_u32 v197, v153, 12, v5
	global_load_dwordx2 v[48:49], v197, s[14:15]
	global_load_dwordx2 v[50:51], v197, s[14:15] offset:512
	global_load_dwordx2 v[52:53], v197, s[14:15] offset:1024
	global_load_dwordx2 v[54:55], v197, s[14:15] offset:1536
	v_lshl_add_u32 v198, v154, 12, v5
	global_load_dwordx2 v[56:57], v198, s[14:15]
	global_load_dwordx2 v[58:59], v198, s[14:15] offset:512
	global_load_dwordx2 v[60:61], v198, s[14:15] offset:1024
	global_load_dwordx2 v[62:63], v198, s[14:15] offset:1536
	v_lshl_add_u32 v199, v155, 12, v5
	global_load_dwordx2 v[64:65], v199, s[14:15]
	global_load_dwordx2 v[66:67], v199, s[14:15] offset:512
	global_load_dwordx2 v[68:69], v199, s[14:15] offset:1024
	global_load_dwordx2 v[70:71], v199, s[14:15] offset:1536
	v_lshl_add_u32 v156, v152, 13, v6
	v_lshl_add_u32 v157, v153, 13, v6
	v_lshl_add_u32 v158, v154, 13, v6
	v_lshl_add_u32 v159, v155, 13, v6
	s_waitcnt vmcnt(16)
	v_lshl_add_u32 v200, v8, 2, s23
	v_lshl_add_u32 v201, v9, 2, s23
	v_lshl_add_u32 v202, v10, 2, s23
	v_lshl_add_u32 v203, v11, 2, s23
	v_lshl_add_u32 v204, v12, 2, s23
	v_lshl_add_u32 v205, v13, 2, s23
	v_lshl_add_u32 v206, v14, 2, s23
	v_lshl_add_u32 v207, v15, 2, s23
	v_lshl_add_u32 v208, v16, 2, s23
	v_lshl_add_u32 v209, v17, 2, s23
	v_lshl_add_u32 v210, v18, 2, s23
	v_lshl_add_u32 v211, v19, 2, s23
	v_lshl_add_u32 v212, v20, 2, s23
	v_lshl_add_u32 v213, v21, 2, s23
	v_lshl_add_u32 v214, v22, 2, s23
	v_lshl_add_u32 v215, v23, 2, s23
	ds_read_b32 v136, v200
	ds_read_b32 v137, v201
	ds_read_b32 v138, v202
	ds_read_b32 v139, v203
	ds_read_b32 v140, v204
	ds_read_b32 v141, v205
	ds_read_b32 v142, v206
	ds_read_b32 v143, v207
	ds_read_b32 v144, v208
	ds_read_b32 v145, v209
	ds_read_b32 v146, v210
	ds_read_b32 v147, v211
	ds_read_b32 v148, v212
	ds_read_b32 v149, v213
	ds_read_b32 v150, v214
	ds_read_b32 v151, v215
	s_waitcnt lgkmcnt(12)
	v_lshl_add_u32 v136, v136, 8, v24
	v_lshl_add_u32 v137, v137, 8, v25
	v_lshl_add_u32 v138, v138, 8, v26
	v_lshl_add_u32 v139, v139, 8, v27
	v_lshl_add_u32 v136, v136, 11, v4
	v_lshl_add_u32 v137, v137, 11, v4
	v_lshl_add_u32 v138, v138, 11, v4
	v_lshl_add_u32 v139, v139, 11, v4
	global_load_dword v72, v136, s[6:7]
	global_load_dword v73, v136, s[6:7] offset:256
	global_load_dword v74, v136, s[6:7] offset:512
	global_load_dword v75, v136, s[6:7] offset:768
	global_load_dword v76, v137, s[6:7]
	global_load_dword v77, v137, s[6:7] offset:256
	global_load_dword v78, v137, s[6:7] offset:512
	global_load_dword v79, v137, s[6:7] offset:768
	global_load_dword v80, v138, s[6:7]
	global_load_dword v81, v138, s[6:7] offset:256
	global_load_dword v82, v138, s[6:7] offset:512
	global_load_dword v83, v138, s[6:7] offset:768
	global_load_dword v84, v139, s[6:7]
	global_load_dword v85, v139, s[6:7] offset:256
	global_load_dword v86, v139, s[6:7] offset:512
	global_load_dword v87, v139, s[6:7] offset:768
	s_waitcnt lgkmcnt(8)
	v_lshl_add_u32 v140, v140, 8, v28
	v_lshl_add_u32 v141, v141, 8, v29
	v_lshl_add_u32 v142, v142, 8, v30
	v_lshl_add_u32 v143, v143, 8, v31
	v_lshl_add_u32 v140, v140, 11, v4
	v_lshl_add_u32 v141, v141, 11, v4
	v_lshl_add_u32 v142, v142, 11, v4
	v_lshl_add_u32 v143, v143, 11, v4
	global_load_dword v88, v140, s[6:7]
	global_load_dword v89, v140, s[6:7] offset:256
	global_load_dword v90, v140, s[6:7] offset:512
	global_load_dword v91, v140, s[6:7] offset:768
	global_load_dword v92, v141, s[6:7]
	global_load_dword v93, v141, s[6:7] offset:256
	global_load_dword v94, v141, s[6:7] offset:512
	global_load_dword v95, v141, s[6:7] offset:768
	global_load_dword v96, v142, s[6:7]
	global_load_dword v97, v142, s[6:7] offset:256
	global_load_dword v98, v142, s[6:7] offset:512
	global_load_dword v99, v142, s[6:7] offset:768
	global_load_dword v100, v143, s[6:7]
	global_load_dword v101, v143, s[6:7] offset:256
	global_load_dword v102, v143, s[6:7] offset:512
	global_load_dword v103, v143, s[6:7] offset:768
	s_waitcnt lgkmcnt(4)
; __device__ __forceinline__ float bf_lo(unsigned w) { return __uint_as_float(w << 16); }
; __device__ __forceinline__ float bf_hi(unsigned w) { return __uint_as_float(w & 0xffff0000u); }
; __global__ void __launch_bounds__(512, 2) fwd_kernel(Params p) {
;     ...
;                 for (int k = 0; k < 4; ++k) { const int pos = ts[ee[u][k]] * 256 + rk[u][k]; y[u][k] = *(const u32x4*)(Yb + (size_t)pos * DM + cc[u]); }
; #pragma unroll
;             for (int u = 0; u < UN; ++u) {
;                 f32x4 a[4];
;                 a[0] = (f32x4){bf_lo(xa[u].x), bf_hi(xa[u].x), bf_lo(xa[u].y), bf_hi(xa[u].y)}; a[1] = (f32x4){bf_lo(xa[u].z), bf_hi(xa[u].z), bf_lo(xa[u].w), bf_hi(xa[u].w)};
;                 a[2] = (f32x4){bf_lo(xb[u].x), bf_hi(xb[u].x), bf_lo(xb[u].y), bf_hi(xb[u].y)}; a[3] = (f32x4){bf_lo(xb[u].z), bf_hi(xb[u].z), bf_lo(xb[u].w), bf_hi(xb[u].w)};
; #pragma unroll
;                 for (int k = 0; k < 4; ++k)
; #pragma unroll
;                     for (int q = 0; q < 4; ++q) { const f32x2 lo = __builtin_amdgcn_cvt_pk_f32_fp8((int)y[u][k][q], false), hi = __builtin_amdgcn_cvt_pk_f32_fp8((int)y[u][k][q], true);
;                         a[q].x += lo.x * (1.0f / Y8_SCALE); a[q].y += lo.y * (1.0f / Y8_SCALE); a[q].z += hi.x * (1.0f / Y8_SCALE); a[q].w += hi.y * (1.0f / Y8_SCALE); }
;                 if (it0 + u * NGT < NI) { float* op = p.out + (size_t)mm[u] * DM + cc[u];
; #pragma unroll
;                     for (int q = 0; q < 4; ++q) *(f32x4*)(op + 4 * q) = a[q]; }
	v_lshl_add_u32 v144, v144, 8, v32
	v_lshl_add_u32 v145, v145, 8, v33
	v_lshl_add_u32 v146, v146, 8, v34
	v_lshl_add_u32 v147, v147, 8, v35
	v_lshl_add_u32 v144, v144, 11, v4
	v_lshl_add_u32 v145, v145, 11, v4
	v_lshl_add_u32 v146, v146, 11, v4
	v_lshl_add_u32 v147, v147, 11, v4
	global_load_dword v104, v144, s[6:7]
	global_load_dword v105, v144, s[6:7] offset:256
	global_load_dword v106, v144, s[6:7] offset:512
	global_load_dword v107, v144, s[6:7] offset:768
	global_load_dword v108, v145, s[6:7]
	global_load_dword v109, v145, s[6:7] offset:256
	global_load_dword v110, v145, s[6:7] offset:512
	global_load_dword v111, v145, s[6:7] offset:768
	global_load_dword v112, v146, s[6:7]
	global_load_dword v113, v146, s[6:7] offset:256
	global_load_dword v114, v146, s[6:7] offset:512
	global_load_dword v115, v146, s[6:7] offset:768
	global_load_dword v116, v147, s[6:7]
	global_load_dword v117, v147, s[6:7] offset:256
	global_load_dword v118, v147, s[6:7] offset:512
	global_load_dword v119, v147, s[6:7] offset:768
	s_waitcnt lgkmcnt(0)
	v_lshl_add_u32 v148, v148, 8, v36
	v_lshl_add_u32 v149, v149, 8, v37
	v_lshl_add_u32 v150, v150, 8, v38
	v_lshl_add_u32 v151, v151, 8, v39
	v_lshl_add_u32 v148, v148, 11, v4
	v_lshl_add_u32 v149, v149, 11, v4
	v_lshl_add_u32 v150, v150, 11, v4
	v_lshl_add_u32 v151, v151, 11, v4
	global_load_dword v120, v148, s[6:7]
	global_load_dword v121, v148, s[6:7] offset:256
	global_load_dword v122, v148, s[6:7] offset:512
	global_load_dword v123, v148, s[6:7] offset:768
	global_load_dword v124, v149, s[6:7]
	global_load_dword v125, v149, s[6:7] offset:256
	global_load_dword v126, v149, s[6:7] offset:512
	global_load_dword v127, v149, s[6:7] offset:768
	global_load_dword v128, v150, s[6:7]
	global_load_dword v129, v150, s[6:7] offset:256
	global_load_dword v130, v150, s[6:7] offset:512
	global_load_dword v131, v150, s[6:7] offset:768
	global_load_dword v132, v151, s[6:7]
	global_load_dword v133, v151, s[6:7] offset:256
	global_load_dword v134, v151, s[6:7] offset:512
	global_load_dword v135, v151, s[6:7] offset:768
	s_waitcnt vmcnt(48)
	v_lshlrev_b32_e32 v176, 16, v40
	v_and_b32_e32 v177, 0xffff0000, v40
	v_lshlrev_b32_e32 v178, 16, v41
	v_and_b32_e32 v179, 0xffff0000, v41
	v_cvt_pk_f32_fp8_e32 v[160:161], v72
	v_cvt_pk_f32_fp8_sdwa v[162:163], v72 src0_sel:WORD_1
	v_pk_fma_f32 v[176:177], v[160:161], s[10:11], v[176:177] op_sel_hi:[1,0,1]
	v_pk_fma_f32 v[178:179], v[162:163], s[10:11], v[178:179] op_sel_hi:[1,0,1]
	v_cvt_pk_f32_fp8_e32 v[164:165], v76
	v_cvt_pk_f32_fp8_sdwa v[166:167], v76 src0_sel:WORD_1
	v_pk_fma_f32 v[176:177], v[164:165], s[10:11], v[176:177] op_sel_hi:[1,0,1]
	v_pk_fma_f32 v[178:179], v[166:167], s[10:11], v[178:179] op_sel_hi:[1,0,1]
	v_cvt_pk_f32_fp8_e32 v[168:169], v80
	v_cvt_pk_f32_fp8_sdwa v[170:171], v80 src0_sel:WORD_1
	v_pk_fma_f32 v[176:177], v[168:169], s[10:11], v[176:177] op_sel_hi:[1,0,1]
	v_pk_fma_f32 v[178:179], v[170:171], s[10:11], v[178:179] op_sel_hi:[1,0,1]
	v_cvt_pk_f32_fp8_e32 v[172:173], v84
	v_cvt_pk_f32_fp8_sdwa v[174:175], v84 src0_sel:WORD_1
	v_pk_fma_f32 v[176:177], v[172:173], s[10:11], v[176:177] op_sel_hi:[1,0,1]
	v_pk_fma_f32 v[178:179], v[174:175], s[10:11], v[178:179] op_sel_hi:[1,0,1]
	global_store_dwordx4 v156, v[176:179], s[4:5]
	v_lshlrev_b32_e32 v180, 16, v42
	v_and_b32_e32 v181, 0xffff0000, v42
	v_lshlrev_b32_e32 v182, 16, v43
	v_and_b32_e32 v183, 0xffff0000, v43
	v_cvt_pk_f32_fp8_e32 v[160:161], v73
	v_cvt_pk_f32_fp8_sdwa v[162:163], v73 src0_sel:WORD_1
	v_pk_fma_f32 v[180:181], v[160:161], s[10:11], v[180:181] op_sel_hi:[1,0,1]
	v_pk_fma_f32 v[182:183], v[162:163], s[10:11], v[182:183] op_sel_hi:[1,0,1]
	v_cvt_pk_f32_fp8_e32 v[164:165], v77
	v_cvt_pk_f32_fp8_sdwa v[166:167], v77 src0_sel:WORD_1
	v_pk_fma_f32 v[180:181], v[164:165], s[10:11], v[180:181] op_sel_hi:[1,0,1]
	v_pk_fma_f32 v[182:183], v[166:167], s[10:11], v[182:183] op_sel_hi:[1,0,1]
	v_cvt_pk_f32_fp8_e32 v[168:169], v81
	v_cvt_pk_f32_fp8_sdwa v[170:171], v81 src0_sel:WORD_1
	v_pk_fma_f32 v[180:181], v[168:169], s[10:11], v[180:181] op_sel_hi:[1,0,1]
	v_pk_fma_f32 v[182:183], v[170:171], s[10:11], v[182:183] op_sel_hi:[1,0,1]
	v_cvt_pk_f32_fp8_e32 v[172:173], v85
	v_cvt_pk_f32_fp8_sdwa v[174:175], v85 src0_sel:WORD_1
	v_pk_fma_f32 v[180:181], v[172:173], s[10:11], v[180:181] op_sel_hi:[1,0,1]
	v_pk_fma_f32 v[182:183], v[174:175], s[10:11], v[182:183] op_sel_hi:[1,0,1]
	global_store_dwordx4 v156, v[180:183], s[4:5] offset:1024
	v_lshlrev_b32_e32 v184, 16, v44
	v_and_b32_e32 v185, 0xffff0000, v44
	v_lshlrev_b32_e32 v186, 16, v45
	v_and_b32_e32 v187, 0xffff0000, v45
	v_cvt_pk_f32_fp8_e32 v[160:161], v74
	v_cvt_pk_f32_fp8_sdwa v[162:163], v74 src0_sel:WORD_1
	v_pk_fma_f32 v[184:185], v[160:161], s[10:11], v[184:185] op_sel_hi:[1,0,1]
	v_pk_fma_f32 v[186:187], v[162:163], s[10:11], v[186:187] op_sel_hi:[1,0,1]
	v_cvt_pk_f32_fp8_e32 v[164:165], v78
	v_cvt_pk_f32_fp8_sdwa v[166:167], v78 src0_sel:WORD_1
	v_pk_fma_f32 v[184:185], v[164:165], s[10:11], v[184:185] op_sel_hi:[1,0,1]
	v_pk_fma_f32 v[186:187], v[166:167], s[10:11], v[186:187] op_sel_hi:[1,0,1]
	v_cvt_pk_f32_fp8_e32 v[168:169], v82
	v_cvt_pk_f32_fp8_sdwa v[170:171], v82 src0_sel:WORD_1
	v_pk_fma_f32 v[184:185], v[168:169], s[10:11], v[184:185] op_sel_hi:[1,0,1]
	v_pk_fma_f32 v[186:187], v[170:171], s[10:11], v[186:187] op_sel_hi:[1,0,1]
	v_cvt_pk_f32_fp8_e32 v[172:173], v86
	v_cvt_pk_f32_fp8_sdwa v[174:175], v86 src0_sel:WORD_1
	v_pk_fma_f32 v[184:185], v[172:173], s[10:11], v[184:185] op_sel_hi:[1,0,1]
	v_pk_fma_f32 v[186:187], v[174:175], s[10:11], v[186:187] op_sel_hi:[1,0,1]
	global_store_dwordx4 v156, v[184:187], s[4:5] offset:2048
	v_lshlrev_b32_e32 v188, 16, v46
	v_and_b32_e32 v189, 0xffff0000, v46
	v_lshlrev_b32_e32 v190, 16, v47
	v_and_b32_e32 v191, 0xffff0000, v47
	v_cvt_pk_f32_fp8_e32 v[160:161], v75
	v_cvt_pk_f32_fp8_sdwa v[162:163], v75 src0_sel:WORD_1
	v_pk_fma_f32 v[188:189], v[160:161], s[10:11], v[188:189] op_sel_hi:[1,0,1]
	v_pk_fma_f32 v[190:191], v[162:163], s[10:11], v[190:191] op_sel_hi:[1,0,1]
	v_cvt_pk_f32_fp8_e32 v[164:165], v79
	v_cvt_pk_f32_fp8_sdwa v[166:167], v79 src0_sel:WORD_1
	v_pk_fma_f32 v[188:189], v[164:165], s[10:11], v[188:189] op_sel_hi:[1,0,1]
	v_pk_fma_f32 v[190:191], v[166:167], s[10:11], v[190:191] op_sel_hi:[1,0,1]
	v_cvt_pk_f32_fp8_e32 v[168:169], v83
	v_cvt_pk_f32_fp8_sdwa v[170:171], v83 src0_sel:WORD_1
	v_pk_fma_f32 v[188:189], v[168:169], s[10:11], v[188:189] op_sel_hi:[1,0,1]
	v_pk_fma_f32 v[190:191], v[170:171], s[10:11], v[190:191] op_sel_hi:[1,0,1]
	v_cvt_pk_f32_fp8_e32 v[172:173], v87
	v_cvt_pk_f32_fp8_sdwa v[174:175], v87 src0_sel:WORD_1
	v_pk_fma_f32 v[188:189], v[172:173], s[10:11], v[188:189] op_sel_hi:[1,0,1]
	v_pk_fma_f32 v[190:191], v[174:175], s[10:11], v[190:191] op_sel_hi:[1,0,1]
	global_store_dwordx4 v156, v[188:191], s[4:5] offset:3072
	s_waitcnt vmcnt(36)
; __device__ __forceinline__ float bf_lo(unsigned w) { return __uint_as_float(w << 16); }
; __device__ __forceinline__ float bf_hi(unsigned w) { return __uint_as_float(w & 0xffff0000u); }
; __global__ void __launch_bounds__(512, 2) fwd_kernel(Params p) {
;     ...
;             for (int u = 0; u < UN; ++u) {
;                 f32x4 a[4];
;                 a[0] = (f32x4){bf_lo(xa[u].x), bf_hi(xa[u].x), bf_lo(xa[u].y), bf_hi(xa[u].y)}; a[1] = (f32x4){bf_lo(xa[u].z), bf_hi(xa[u].z), bf_lo(xa[u].w), bf_hi(xa[u].w)};
;                 a[2] = (f32x4){bf_lo(xb[u].x), bf_hi(xb[u].x), bf_lo(xb[u].y), bf_hi(xb[u].y)}; a[3] = (f32x4){bf_lo(xb[u].z), bf_hi(xb[u].z), bf_lo(xb[u].w), bf_hi(xb[u].w)};
; #pragma unroll
;                 for (int k = 0; k < 4; ++k)
; #pragma unroll
;                     for (int q = 0; q < 4; ++q) { const f32x2 lo = __builtin_amdgcn_cvt_pk_f32_fp8((int)y[u][k][q], false), hi = __builtin_amdgcn_cvt_pk_f32_fp8((int)y[u][k][q], true);
;                         a[q].x += lo.x * (1.0f / Y8_SCALE); a[q].y += lo.y * (1.0f / Y8_SCALE); a[q].z += hi.x * (1.0f / Y8_SCALE); a[q].w += hi.y * (1.0f / Y8_SCALE); }
;                 if (it0 + u * NGT < NI) { float* op = p.out + (size_t)mm[u] * DM + cc[u];
; #pragma unroll
;                     for (int q = 0; q < 4; ++q) *(f32x4*)(op + 4 * q) = a[q]; }
	v_lshlrev_b32_e32 v176, 16, v48
	v_and_b32_e32 v177, 0xffff0000, v48
	v_lshlrev_b32_e32 v178, 16, v49
	v_and_b32_e32 v179, 0xffff0000, v49
	v_cvt_pk_f32_fp8_e32 v[160:161], v88
	v_cvt_pk_f32_fp8_sdwa v[162:163], v88 src0_sel:WORD_1
	v_pk_fma_f32 v[176:177], v[160:161], s[10:11], v[176:177] op_sel_hi:[1,0,1]
	v_pk_fma_f32 v[178:179], v[162:163], s[10:11], v[178:179] op_sel_hi:[1,0,1]
	v_cvt_pk_f32_fp8_e32 v[164:165], v92
	v_cvt_pk_f32_fp8_sdwa v[166:167], v92 src0_sel:WORD_1
	v_pk_fma_f32 v[176:177], v[164:165], s[10:11], v[176:177] op_sel_hi:[1,0,1]
	v_pk_fma_f32 v[178:179], v[166:167], s[10:11], v[178:179] op_sel_hi:[1,0,1]
	v_cvt_pk_f32_fp8_e32 v[168:169], v96
	v_cvt_pk_f32_fp8_sdwa v[170:171], v96 src0_sel:WORD_1
	v_pk_fma_f32 v[176:177], v[168:169], s[10:11], v[176:177] op_sel_hi:[1,0,1]
	v_pk_fma_f32 v[178:179], v[170:171], s[10:11], v[178:179] op_sel_hi:[1,0,1]
	v_cvt_pk_f32_fp8_e32 v[172:173], v100
	v_cvt_pk_f32_fp8_sdwa v[174:175], v100 src0_sel:WORD_1
	v_pk_fma_f32 v[176:177], v[172:173], s[10:11], v[176:177] op_sel_hi:[1,0,1]
	v_pk_fma_f32 v[178:179], v[174:175], s[10:11], v[178:179] op_sel_hi:[1,0,1]
	global_store_dwordx4 v157, v[176:179], s[4:5]
	v_lshlrev_b32_e32 v180, 16, v50
	v_and_b32_e32 v181, 0xffff0000, v50
	v_lshlrev_b32_e32 v182, 16, v51
	v_and_b32_e32 v183, 0xffff0000, v51
	v_cvt_pk_f32_fp8_e32 v[160:161], v89
	v_cvt_pk_f32_fp8_sdwa v[162:163], v89 src0_sel:WORD_1
	v_pk_fma_f32 v[180:181], v[160:161], s[10:11], v[180:181] op_sel_hi:[1,0,1]
	v_pk_fma_f32 v[182:183], v[162:163], s[10:11], v[182:183] op_sel_hi:[1,0,1]
	v_cvt_pk_f32_fp8_e32 v[164:165], v93
	v_cvt_pk_f32_fp8_sdwa v[166:167], v93 src0_sel:WORD_1
	v_pk_fma_f32 v[180:181], v[164:165], s[10:11], v[180:181] op_sel_hi:[1,0,1]
	v_pk_fma_f32 v[182:183], v[166:167], s[10:11], v[182:183] op_sel_hi:[1,0,1]
	v_cvt_pk_f32_fp8_e32 v[168:169], v97
	v_cvt_pk_f32_fp8_sdwa v[170:171], v97 src0_sel:WORD_1
	v_pk_fma_f32 v[180:181], v[168:169], s[10:11], v[180:181] op_sel_hi:[1,0,1]
	v_pk_fma_f32 v[182:183], v[170:171], s[10:11], v[182:183] op_sel_hi:[1,0,1]
	v_cvt_pk_f32_fp8_e32 v[172:173], v101
	v_cvt_pk_f32_fp8_sdwa v[174:175], v101 src0_sel:WORD_1
	v_pk_fma_f32 v[180:181], v[172:173], s[10:11], v[180:181] op_sel_hi:[1,0,1]
	v_pk_fma_f32 v[182:183], v[174:175], s[10:11], v[182:183] op_sel_hi:[1,0,1]
	global_store_dwordx4 v157, v[180:183], s[4:5] offset:1024
	v_lshlrev_b32_e32 v184, 16, v52
	v_and_b32_e32 v185, 0xffff0000, v52
	v_lshlrev_b32_e32 v186, 16, v53
	v_and_b32_e32 v187, 0xffff0000, v53
	v_cvt_pk_f32_fp8_e32 v[160:161], v90
	v_cvt_pk_f32_fp8_sdwa v[162:163], v90 src0_sel:WORD_1
	v_pk_fma_f32 v[184:185], v[160:161], s[10:11], v[184:185] op_sel_hi:[1,0,1]
	v_pk_fma_f32 v[186:187], v[162:163], s[10:11], v[186:187] op_sel_hi:[1,0,1]
	v_cvt_pk_f32_fp8_e32 v[164:165], v94
	v_cvt_pk_f32_fp8_sdwa v[166:167], v94 src0_sel:WORD_1
	v_pk_fma_f32 v[184:185], v[164:165], s[10:11], v[184:185] op_sel_hi:[1,0,1]
	v_pk_fma_f32 v[186:187], v[166:167], s[10:11], v[186:187] op_sel_hi:[1,0,1]
	v_cvt_pk_f32_fp8_e32 v[168:169], v98
	v_cvt_pk_f32_fp8_sdwa v[170:171], v98 src0_sel:WORD_1
	v_pk_fma_f32 v[184:185], v[168:169], s[10:11], v[184:185] op_sel_hi:[1,0,1]
	v_pk_fma_f32 v[186:187], v[170:171], s[10:11], v[186:187] op_sel_hi:[1,0,1]
	v_cvt_pk_f32_fp8_e32 v[172:173], v102
	v_cvt_pk_f32_fp8_sdwa v[174:175], v102 src0_sel:WORD_1
	v_pk_fma_f32 v[184:185], v[172:173], s[10:11], v[184:185] op_sel_hi:[1,0,1]
	v_pk_fma_f32 v[186:187], v[174:175], s[10:11], v[186:187] op_sel_hi:[1,0,1]
	global_store_dwordx4 v157, v[184:187], s[4:5] offset:2048
	v_lshlrev_b32_e32 v188, 16, v54
	v_and_b32_e32 v189, 0xffff0000, v54
	v_lshlrev_b32_e32 v190, 16, v55
	v_and_b32_e32 v191, 0xffff0000, v55
	v_cvt_pk_f32_fp8_e32 v[160:161], v91
	v_cvt_pk_f32_fp8_sdwa v[162:163], v91 src0_sel:WORD_1
	v_pk_fma_f32 v[188:189], v[160:161], s[10:11], v[188:189] op_sel_hi:[1,0,1]
	v_pk_fma_f32 v[190:191], v[162:163], s[10:11], v[190:191] op_sel_hi:[1,0,1]
	v_cvt_pk_f32_fp8_e32 v[164:165], v95
	v_cvt_pk_f32_fp8_sdwa v[166:167], v95 src0_sel:WORD_1
	v_pk_fma_f32 v[188:189], v[164:165], s[10:11], v[188:189] op_sel_hi:[1,0,1]
	v_pk_fma_f32 v[190:191], v[166:167], s[10:11], v[190:191] op_sel_hi:[1,0,1]
	v_cvt_pk_f32_fp8_e32 v[168:169], v99
	v_cvt_pk_f32_fp8_sdwa v[170:171], v99 src0_sel:WORD_1
	v_pk_fma_f32 v[188:189], v[168:169], s[10:11], v[188:189] op_sel_hi:[1,0,1]
	v_pk_fma_f32 v[190:191], v[170:171], s[10:11], v[190:191] op_sel_hi:[1,0,1]
	v_cvt_pk_f32_fp8_e32 v[172:173], v103
	v_cvt_pk_f32_fp8_sdwa v[174:175], v103 src0_sel:WORD_1
	v_pk_fma_f32 v[188:189], v[172:173], s[10:11], v[188:189] op_sel_hi:[1,0,1]
	v_pk_fma_f32 v[190:191], v[174:175], s[10:11], v[190:191] op_sel_hi:[1,0,1]
	global_store_dwordx4 v157, v[188:191], s[4:5] offset:3072
	s_waitcnt vmcnt(24)
; __device__ __forceinline__ float bf_lo(unsigned w) { return __uint_as_float(w << 16); }
; __device__ __forceinline__ float bf_hi(unsigned w) { return __uint_as_float(w & 0xffff0000u); }
; __global__ void __launch_bounds__(512, 2) fwd_kernel(Params p) {
;     ...
;             for (int u = 0; u < UN; ++u) {
;                 f32x4 a[4];
;                 a[0] = (f32x4){bf_lo(xa[u].x), bf_hi(xa[u].x), bf_lo(xa[u].y), bf_hi(xa[u].y)}; a[1] = (f32x4){bf_lo(xa[u].z), bf_hi(xa[u].z), bf_lo(xa[u].w), bf_hi(xa[u].w)};
;                 a[2] = (f32x4){bf_lo(xb[u].x), bf_hi(xb[u].x), bf_lo(xb[u].y), bf_hi(xb[u].y)}; a[3] = (f32x4){bf_lo(xb[u].z), bf_hi(xb[u].z), bf_lo(xb[u].w), bf_hi(xb[u].w)};
; #pragma unroll
;                 for (int k = 0; k < 4; ++k)
; #pragma unroll
;                     for (int q = 0; q < 4; ++q) { const f32x2 lo = __builtin_amdgcn_cvt_pk_f32_fp8((int)y[u][k][q], false), hi = __builtin_amdgcn_cvt_pk_f32_fp8((int)y[u][k][q], true);
;                         a[q].x += lo.x * (1.0f / Y8_SCALE); a[q].y += lo.y * (1.0f / Y8_SCALE); a[q].z += hi.x * (1.0f / Y8_SCALE); a[q].w += hi.y * (1.0f / Y8_SCALE); }
;                 if (it0 + u * NGT < NI) { float* op = p.out + (size_t)mm[u] * DM + cc[u];
; #pragma unroll
;                     for (int q = 0; q < 4; ++q) *(f32x4*)(op + 4 * q) = a[q]; }
	v_lshlrev_b32_e32 v176, 16, v56
	v_and_b32_e32 v177, 0xffff0000, v56
	v_lshlrev_b32_e32 v178, 16, v57
	v_and_b32_e32 v179, 0xffff0000, v57
	v_cvt_pk_f32_fp8_e32 v[160:161], v104
	v_cvt_pk_f32_fp8_sdwa v[162:163], v104 src0_sel:WORD_1
	v_pk_fma_f32 v[176:177], v[160:161], s[10:11], v[176:177] op_sel_hi:[1,0,1]
	v_pk_fma_f32 v[178:179], v[162:163], s[10:11], v[178:179] op_sel_hi:[1,0,1]
	v_cvt_pk_f32_fp8_e32 v[164:165], v108
	v_cvt_pk_f32_fp8_sdwa v[166:167], v108 src0_sel:WORD_1
	v_pk_fma_f32 v[176:177], v[164:165], s[10:11], v[176:177] op_sel_hi:[1,0,1]
	v_pk_fma_f32 v[178:179], v[166:167], s[10:11], v[178:179] op_sel_hi:[1,0,1]
	v_cvt_pk_f32_fp8_e32 v[168:169], v112
	v_cvt_pk_f32_fp8_sdwa v[170:171], v112 src0_sel:WORD_1
	v_pk_fma_f32 v[176:177], v[168:169], s[10:11], v[176:177] op_sel_hi:[1,0,1]
	v_pk_fma_f32 v[178:179], v[170:171], s[10:11], v[178:179] op_sel_hi:[1,0,1]
	v_cvt_pk_f32_fp8_e32 v[172:173], v116
	v_cvt_pk_f32_fp8_sdwa v[174:175], v116 src0_sel:WORD_1
	v_pk_fma_f32 v[176:177], v[172:173], s[10:11], v[176:177] op_sel_hi:[1,0,1]
	v_pk_fma_f32 v[178:179], v[174:175], s[10:11], v[178:179] op_sel_hi:[1,0,1]
	global_store_dwordx4 v158, v[176:179], s[4:5]
	v_lshlrev_b32_e32 v180, 16, v58
	v_and_b32_e32 v181, 0xffff0000, v58
	v_lshlrev_b32_e32 v182, 16, v59
	v_and_b32_e32 v183, 0xffff0000, v59
	v_cvt_pk_f32_fp8_e32 v[160:161], v105
	v_cvt_pk_f32_fp8_sdwa v[162:163], v105 src0_sel:WORD_1
	v_pk_fma_f32 v[180:181], v[160:161], s[10:11], v[180:181] op_sel_hi:[1,0,1]
	v_pk_fma_f32 v[182:183], v[162:163], s[10:11], v[182:183] op_sel_hi:[1,0,1]
	v_cvt_pk_f32_fp8_e32 v[164:165], v109
	v_cvt_pk_f32_fp8_sdwa v[166:167], v109 src0_sel:WORD_1
	v_pk_fma_f32 v[180:181], v[164:165], s[10:11], v[180:181] op_sel_hi:[1,0,1]
	v_pk_fma_f32 v[182:183], v[166:167], s[10:11], v[182:183] op_sel_hi:[1,0,1]
	v_cvt_pk_f32_fp8_e32 v[168:169], v113
	v_cvt_pk_f32_fp8_sdwa v[170:171], v113 src0_sel:WORD_1
	v_pk_fma_f32 v[180:181], v[168:169], s[10:11], v[180:181] op_sel_hi:[1,0,1]
	v_pk_fma_f32 v[182:183], v[170:171], s[10:11], v[182:183] op_sel_hi:[1,0,1]
	v_cvt_pk_f32_fp8_e32 v[172:173], v117
	v_cvt_pk_f32_fp8_sdwa v[174:175], v117 src0_sel:WORD_1
	v_pk_fma_f32 v[180:181], v[172:173], s[10:11], v[180:181] op_sel_hi:[1,0,1]
	v_pk_fma_f32 v[182:183], v[174:175], s[10:11], v[182:183] op_sel_hi:[1,0,1]
	global_store_dwordx4 v158, v[180:183], s[4:5] offset:1024
	v_lshlrev_b32_e32 v184, 16, v60
	v_and_b32_e32 v185, 0xffff0000, v60
	v_lshlrev_b32_e32 v186, 16, v61
	v_and_b32_e32 v187, 0xffff0000, v61
	v_cvt_pk_f32_fp8_e32 v[160:161], v106
	v_cvt_pk_f32_fp8_sdwa v[162:163], v106 src0_sel:WORD_1
	v_pk_fma_f32 v[184:185], v[160:161], s[10:11], v[184:185] op_sel_hi:[1,0,1]
	v_pk_fma_f32 v[186:187], v[162:163], s[10:11], v[186:187] op_sel_hi:[1,0,1]
	v_cvt_pk_f32_fp8_e32 v[164:165], v110
	v_cvt_pk_f32_fp8_sdwa v[166:167], v110 src0_sel:WORD_1
	v_pk_fma_f32 v[184:185], v[164:165], s[10:11], v[184:185] op_sel_hi:[1,0,1]
	v_pk_fma_f32 v[186:187], v[166:167], s[10:11], v[186:187] op_sel_hi:[1,0,1]
	v_cvt_pk_f32_fp8_e32 v[168:169], v114
	v_cvt_pk_f32_fp8_sdwa v[170:171], v114 src0_sel:WORD_1
	v_pk_fma_f32 v[184:185], v[168:169], s[10:11], v[184:185] op_sel_hi:[1,0,1]
	v_pk_fma_f32 v[186:187], v[170:171], s[10:11], v[186:187] op_sel_hi:[1,0,1]
	v_cvt_pk_f32_fp8_e32 v[172:173], v118
	v_cvt_pk_f32_fp8_sdwa v[174:175], v118 src0_sel:WORD_1
	v_pk_fma_f32 v[184:185], v[172:173], s[10:11], v[184:185] op_sel_hi:[1,0,1]
	v_pk_fma_f32 v[186:187], v[174:175], s[10:11], v[186:187] op_sel_hi:[1,0,1]
	global_store_dwordx4 v158, v[184:187], s[4:5] offset:2048
	v_lshlrev_b32_e32 v188, 16, v62
	v_and_b32_e32 v189, 0xffff0000, v62
	v_lshlrev_b32_e32 v190, 16, v63
	v_and_b32_e32 v191, 0xffff0000, v63
	v_cvt_pk_f32_fp8_e32 v[160:161], v107
	v_cvt_pk_f32_fp8_sdwa v[162:163], v107 src0_sel:WORD_1
	v_pk_fma_f32 v[188:189], v[160:161], s[10:11], v[188:189] op_sel_hi:[1,0,1]
	v_pk_fma_f32 v[190:191], v[162:163], s[10:11], v[190:191] op_sel_hi:[1,0,1]
	v_cvt_pk_f32_fp8_e32 v[164:165], v111
	v_cvt_pk_f32_fp8_sdwa v[166:167], v111 src0_sel:WORD_1
	v_pk_fma_f32 v[188:189], v[164:165], s[10:11], v[188:189] op_sel_hi:[1,0,1]
	v_pk_fma_f32 v[190:191], v[166:167], s[10:11], v[190:191] op_sel_hi:[1,0,1]
	v_cvt_pk_f32_fp8_e32 v[168:169], v115
	v_cvt_pk_f32_fp8_sdwa v[170:171], v115 src0_sel:WORD_1
	v_pk_fma_f32 v[188:189], v[168:169], s[10:11], v[188:189] op_sel_hi:[1,0,1]
	v_pk_fma_f32 v[190:191], v[170:171], s[10:11], v[190:191] op_sel_hi:[1,0,1]
	v_cvt_pk_f32_fp8_e32 v[172:173], v119
	v_cvt_pk_f32_fp8_sdwa v[174:175], v119 src0_sel:WORD_1
	v_pk_fma_f32 v[188:189], v[172:173], s[10:11], v[188:189] op_sel_hi:[1,0,1]
	v_pk_fma_f32 v[190:191], v[174:175], s[10:11], v[190:191] op_sel_hi:[1,0,1]
	global_store_dwordx4 v158, v[188:191], s[4:5] offset:3072
	s_waitcnt vmcnt(12)
; __device__ __forceinline__ float bf_lo(unsigned w) { return __uint_as_float(w << 16); }
; __device__ __forceinline__ float bf_hi(unsigned w) { return __uint_as_float(w & 0xffff0000u); }
; __global__ void __launch_bounds__(512, 2) fwd_kernel(Params p) {
;     ...
;             for (int u = 0; u < UN; ++u) {
;                 f32x4 a[4];
;                 a[0] = (f32x4){bf_lo(xa[u].x), bf_hi(xa[u].x), bf_lo(xa[u].y), bf_hi(xa[u].y)}; a[1] = (f32x4){bf_lo(xa[u].z), bf_hi(xa[u].z), bf_lo(xa[u].w), bf_hi(xa[u].w)};
;                 a[2] = (f32x4){bf_lo(xb[u].x), bf_hi(xb[u].x), bf_lo(xb[u].y), bf_hi(xb[u].y)}; a[3] = (f32x4){bf_lo(xb[u].z), bf_hi(xb[u].z), bf_lo(xb[u].w), bf_hi(xb[u].w)};
; #pragma unroll
;                 for (int k = 0; k < 4; ++k)
; #pragma unroll
;                     for (int q = 0; q < 4; ++q) { const f32x2 lo = __builtin_amdgcn_cvt_pk_f32_fp8((int)y[u][k][q], false), hi = __builtin_amdgcn_cvt_pk_f32_fp8((int)y[u][k][q], true);
;                         a[q].x += lo.x * (1.0f / Y8_SCALE); a[q].y += lo.y * (1.0f / Y8_SCALE); a[q].z += hi.x * (1.0f / Y8_SCALE); a[q].w += hi.y * (1.0f / Y8_SCALE); }
;                 if (it0 + u * NGT < NI) { float* op = p.out + (size_t)mm[u] * DM + cc[u];
; #pragma unroll
;                     for (int q = 0; q < 4; ++q) *(f32x4*)(op + 4 * q) = a[q]; }
;             }
;         }
	v_lshlrev_b32_e32 v176, 16, v64
	v_and_b32_e32 v177, 0xffff0000, v64
	v_lshlrev_b32_e32 v178, 16, v65
	v_and_b32_e32 v179, 0xffff0000, v65
	v_cvt_pk_f32_fp8_e32 v[160:161], v120
	v_cvt_pk_f32_fp8_sdwa v[162:163], v120 src0_sel:WORD_1
	v_pk_fma_f32 v[176:177], v[160:161], s[10:11], v[176:177] op_sel_hi:[1,0,1]
	v_pk_fma_f32 v[178:179], v[162:163], s[10:11], v[178:179] op_sel_hi:[1,0,1]
	v_cvt_pk_f32_fp8_e32 v[164:165], v124
	v_cvt_pk_f32_fp8_sdwa v[166:167], v124 src0_sel:WORD_1
	v_pk_fma_f32 v[176:177], v[164:165], s[10:11], v[176:177] op_sel_hi:[1,0,1]
	v_pk_fma_f32 v[178:179], v[166:167], s[10:11], v[178:179] op_sel_hi:[1,0,1]
	v_cvt_pk_f32_fp8_e32 v[168:169], v128
	v_cvt_pk_f32_fp8_sdwa v[170:171], v128 src0_sel:WORD_1
	v_pk_fma_f32 v[176:177], v[168:169], s[10:11], v[176:177] op_sel_hi:[1,0,1]
	v_pk_fma_f32 v[178:179], v[170:171], s[10:11], v[178:179] op_sel_hi:[1,0,1]
	v_cvt_pk_f32_fp8_e32 v[172:173], v132
	v_cvt_pk_f32_fp8_sdwa v[174:175], v132 src0_sel:WORD_1
	v_pk_fma_f32 v[176:177], v[172:173], s[10:11], v[176:177] op_sel_hi:[1,0,1]
	v_pk_fma_f32 v[178:179], v[174:175], s[10:11], v[178:179] op_sel_hi:[1,0,1]
	global_store_dwordx4 v159, v[176:179], s[4:5]
	v_lshlrev_b32_e32 v180, 16, v66
	v_and_b32_e32 v181, 0xffff0000, v66
	v_lshlrev_b32_e32 v182, 16, v67
	v_and_b32_e32 v183, 0xffff0000, v67
	v_cvt_pk_f32_fp8_e32 v[160:161], v121
	v_cvt_pk_f32_fp8_sdwa v[162:163], v121 src0_sel:WORD_1
	v_pk_fma_f32 v[180:181], v[160:161], s[10:11], v[180:181] op_sel_hi:[1,0,1]
	v_pk_fma_f32 v[182:183], v[162:163], s[10:11], v[182:183] op_sel_hi:[1,0,1]
	v_cvt_pk_f32_fp8_e32 v[164:165], v125
	v_cvt_pk_f32_fp8_sdwa v[166:167], v125 src0_sel:WORD_1
	v_pk_fma_f32 v[180:181], v[164:165], s[10:11], v[180:181] op_sel_hi:[1,0,1]
	v_pk_fma_f32 v[182:183], v[166:167], s[10:11], v[182:183] op_sel_hi:[1,0,1]
	v_cvt_pk_f32_fp8_e32 v[168:169], v129
	v_cvt_pk_f32_fp8_sdwa v[170:171], v129 src0_sel:WORD_1
	v_pk_fma_f32 v[180:181], v[168:169], s[10:11], v[180:181] op_sel_hi:[1,0,1]
	v_pk_fma_f32 v[182:183], v[170:171], s[10:11], v[182:183] op_sel_hi:[1,0,1]
	v_cvt_pk_f32_fp8_e32 v[172:173], v133
	v_cvt_pk_f32_fp8_sdwa v[174:175], v133 src0_sel:WORD_1
	v_pk_fma_f32 v[180:181], v[172:173], s[10:11], v[180:181] op_sel_hi:[1,0,1]
	v_pk_fma_f32 v[182:183], v[174:175], s[10:11], v[182:183] op_sel_hi:[1,0,1]
	global_store_dwordx4 v159, v[180:183], s[4:5] offset:1024
	v_lshlrev_b32_e32 v184, 16, v68
	v_and_b32_e32 v185, 0xffff0000, v68
	v_lshlrev_b32_e32 v186, 16, v69
	v_and_b32_e32 v187, 0xffff0000, v69
	v_cvt_pk_f32_fp8_e32 v[160:161], v122
	v_cvt_pk_f32_fp8_sdwa v[162:163], v122 src0_sel:WORD_1
	v_pk_fma_f32 v[184:185], v[160:161], s[10:11], v[184:185] op_sel_hi:[1,0,1]
	v_pk_fma_f32 v[186:187], v[162:163], s[10:11], v[186:187] op_sel_hi:[1,0,1]
	v_cvt_pk_f32_fp8_e32 v[164:165], v126
	v_cvt_pk_f32_fp8_sdwa v[166:167], v126 src0_sel:WORD_1
	v_pk_fma_f32 v[184:185], v[164:165], s[10:11], v[184:185] op_sel_hi:[1,0,1]
	v_pk_fma_f32 v[186:187], v[166:167], s[10:11], v[186:187] op_sel_hi:[1,0,1]
	v_cvt_pk_f32_fp8_e32 v[168:169], v130
	v_cvt_pk_f32_fp8_sdwa v[170:171], v130 src0_sel:WORD_1
	v_pk_fma_f32 v[184:185], v[168:169], s[10:11], v[184:185] op_sel_hi:[1,0,1]
	v_pk_fma_f32 v[186:187], v[170:171], s[10:11], v[186:187] op_sel_hi:[1,0,1]
	v_cvt_pk_f32_fp8_e32 v[172:173], v134
	v_cvt_pk_f32_fp8_sdwa v[174:175], v134 src0_sel:WORD_1
	v_pk_fma_f32 v[184:185], v[172:173], s[10:11], v[184:185] op_sel_hi:[1,0,1]
	v_pk_fma_f32 v[186:187], v[174:175], s[10:11], v[186:187] op_sel_hi:[1,0,1]
	global_store_dwordx4 v159, v[184:187], s[4:5] offset:2048
	v_lshlrev_b32_e32 v188, 16, v70
	v_and_b32_e32 v189, 0xffff0000, v70
	v_lshlrev_b32_e32 v190, 16, v71
	v_and_b32_e32 v191, 0xffff0000, v71
	v_cvt_pk_f32_fp8_e32 v[160:161], v123
	v_cvt_pk_f32_fp8_sdwa v[162:163], v123 src0_sel:WORD_1
	v_pk_fma_f32 v[188:189], v[160:161], s[10:11], v[188:189] op_sel_hi:[1,0,1]
	v_pk_fma_f32 v[190:191], v[162:163], s[10:11], v[190:191] op_sel_hi:[1,0,1]
	v_cvt_pk_f32_fp8_e32 v[164:165], v127
	v_cvt_pk_f32_fp8_sdwa v[166:167], v127 src0_sel:WORD_1
	v_pk_fma_f32 v[188:189], v[164:165], s[10:11], v[188:189] op_sel_hi:[1,0,1]
	v_pk_fma_f32 v[190:191], v[166:167], s[10:11], v[190:191] op_sel_hi:[1,0,1]
	v_cvt_pk_f32_fp8_e32 v[168:169], v131
	v_cvt_pk_f32_fp8_sdwa v[170:171], v131 src0_sel:WORD_1
	v_pk_fma_f32 v[188:189], v[168:169], s[10:11], v[188:189] op_sel_hi:[1,0,1]
	v_pk_fma_f32 v[190:191], v[170:171], s[10:11], v[190:191] op_sel_hi:[1,0,1]
	v_cvt_pk_f32_fp8_e32 v[172:173], v135
	v_cvt_pk_f32_fp8_sdwa v[174:175], v135 src0_sel:WORD_1
	v_pk_fma_f32 v[188:189], v[172:173], s[10:11], v[188:189] op_sel_hi:[1,0,1]
	v_pk_fma_f32 v[190:191], v[174:175], s[10:11], v[190:191] op_sel_hi:[1,0,1]
	global_store_dwordx4 v159, v[188:191], s[4:5] offset:3072
	v_add_u32_e32 v3, 0x1000, v3
	s_add_i32 s0, s0, 1
	s_cmp_lt_i32 s0, 4
	s_cbranch_scc1 .Lp12n_loop
	s_branch .LBB0_1207
.Lp12n_orig:
	s_load_dwordx2 s[4:5], s[88:89], 0xb0
	s_lshl_b32 s20, s33, 11
	v_lshlrev_b32_e32 v89, 4, v88
	s_lshl_b32 s21, s33, 15
	s_lshl_b32 s22, s33, 10
	s_mulk_i32 s33, 0x600
	s_mov_b64 s[8:9], 0
	s_waitcnt vmcnt(5)
	v_mov_b32_e32 v73, 0
	s_add_i32 s23, 0, 0x25100
	s_mov_b32 s10, 0x3d800000
	s_mov_b32 s24, 0x1fffff
	s_branch .LBB0_1201
